# hoist LN gain/bias loads out of token loops in ln_in and final (no vmcnt(0) store-load chains)
# baseline (speedup 1.0000x reference)
; #define OPAQUE_TID(P) (((P).wid0 << 6) | lane_id_now())
; DI void ln_row_store(const float (&v)[32], int lane, const float* g, const float* b, float* outf, bf16_t* outb) {
;     ...
;     const int c = (i * 64 + lane) * 4;
;     const float4 gg = *(const float4*)(g + c);
;     const float4 bb = *(const float4*)(b + c);
; DI void phase_ln_in(const Params& p, int bid, int nb) {
;   const int tid_ = OPAQUE_TID(p), lane = tid_ & 63, wv = tid_ >> 6;
;   for (int t = bid * NWAVES + wv; t < NTOK; t += nb * NWAVES) {
;     float v[32];
;     const float* xr = p.x + (size_t)t * DM;
; #pragma unroll
;     for (int i = 0; i < 8; ++i) {
;       const float4 a = *(const float4*)(xr + (i * 64 + lane) * 4);
.LBB0_13:
	s_or_b64 exec, exec, s[2:3]
	v_readlane_b32 s0, v254, 14
	s_lshl_b32 s2, s97, 3
	v_mbcnt_lo_u32_b32 v22, -1, 0
	v_mbcnt_hi_u32_b32 v22, -1, v22
	s_nop 0
	v_or_b32_e32 v0, s0, v22
	s_mov_b32 s0, s2
	v_ashrrev_i32_e32 v20, 6, v0
	v_writelane_b32 v254, s0, 54
	v_add_u32_e32 v56, s2, v20
	s_nop 0
	v_writelane_b32 v254, s1, 55
	s_movk_i32 s0, 0x2000
	v_cmp_gt_i32_e32 vcc, s0, v56
	s_and_saveexec_b64 s[22:23], vcc
	s_cbranch_execz .LBB0_18
	v_mbcnt_lo_u32_b32 v0, -1, 0
	v_mbcnt_hi_u32_b32 v0, -1, v0
	v_and_b32_e32 v1, 64, v0
	v_add_u32_e32 v1, 64, v1
	v_xor_b32_e32 v2, 32, v0
	v_cmp_lt_i32_e32 vcc, v2, v1
	s_lshl_b32 s26, s96, 3
	v_mov_b32_e32 v19, 0
	v_cndmask_b32_e32 v2, v0, v2, vcc
	v_lshlrev_b32_e32 v57, 2, v2
	v_xor_b32_e32 v2, 16, v0
	v_cmp_lt_i32_e32 vcc, v2, v1
	s_cmp_lg_u64 s[68:69], 0
	v_mov_b32_e32 v7, v19
	v_cndmask_b32_e32 v2, v0, v2, vcc
	v_lshlrev_b32_e32 v58, 2, v2
	v_xor_b32_e32 v2, 8, v0
	v_cmp_lt_i32_e32 vcc, v2, v1
	v_mov_b32_e32 v11, v19
	v_mov_b32_e32 v15, v19
	v_cndmask_b32_e32 v2, v0, v2, vcc
	v_lshlrev_b32_e32 v59, 2, v2
	v_xor_b32_e32 v2, 4, v0
	v_cmp_lt_i32_e32 vcc, v2, v1
	v_readlane_b32 s2, v254, 54
	s_cselect_b64 s[0:1], -1, 0
	v_cndmask_b32_e32 v2, v0, v2, vcc
	v_lshlrev_b32_e32 v60, 2, v2
	v_xor_b32_e32 v2, 2, v0
	v_cmp_lt_i32_e32 vcc, v2, v1
	v_ashrrev_i32_e32 v21, 31, v20
	v_readlane_b32 s3, v254, 55
	v_cndmask_b32_e32 v2, v0, v2, vcc
	v_lshlrev_b32_e32 v61, 2, v2
	v_xor_b32_e32 v2, 1, v0
	v_cmp_lt_i32_e32 vcc, v2, v1
	v_and_b32_e32 v26, 63, v22
	s_ashr_i32 s27, s26, 31
	v_cndmask_b32_e32 v0, v0, v2, vcc
	v_lshlrev_b32_e32 v62, 2, v0
	v_lshlrev_b32_e32 v0, 4, v22
	v_and_b32_e32 v18, 0x3f0, v0
	v_lshl_add_u64 v[0:1], s[8:9], 0, v[18:19]
	v_lshl_add_u64 v[2:3], s[10:11], 0, v[18:19]
	v_or_b32_e32 v6, 0x1000, v18
	v_or_b32_e32 v10, 0x1400, v18
	v_or_b32_e32 v14, 0x1800, v18
	v_or_b32_e32 v18, 0x1c00, v18
	v_lshl_add_u64 v[4:5], s[8:9], 0, v[6:7]
	v_lshl_add_u64 v[8:9], s[8:9], 0, v[10:11]
	v_lshl_add_u64 v[12:13], s[8:9], 0, v[14:15]
	v_lshl_add_u64 v[16:17], s[8:9], 0, v[18:19]
	s_mov_b32 s8, s2
	s_ashr_i32 s9, s2, 31
	v_lshl_add_u64 v[24:25], v[20:21], 0, s[8:9]
	v_lshlrev_b64 v[20:21], 13, v[24:25]
	v_writelane_b32 v254, s2, 54
	v_lshl_or_b32 v20, v26, 4, v20
	v_lshlrev_b64 v[22:23], 12, v[24:25]
	v_writelane_b32 v254, s3, 55
	v_lshl_add_u64 v[20:21], s[4:5], 0, v[20:21]
	s_mov_b64 s[2:3], 0x1000
	v_lshl_or_b32 v22, v26, 3, v22
	v_cndmask_b32_e64 v24, 0, 1, s[0:1]
	s_mov_b64 s[28:29], 0
	v_lshl_add_u64 v[6:7], s[10:11], 0, v[6:7]
	v_lshl_add_u64 v[10:11], s[10:11], 0, v[10:11]
	v_lshl_add_u64 v[14:15], s[10:11], 0, v[14:15]
	v_lshl_add_u64 v[18:19], s[10:11], 0, v[18:19]
	v_lshl_add_u64 v[20:21], v[20:21], 0, s[2:3]
	s_lshl_b64 s[4:5], s[26:27], 13
	v_lshl_add_u64 v[22:23], s[68:69], 0, v[22:23]
	s_lshl_b64 s[8:9], s[26:27], 12
	v_mov_b32_e32 v63, 0x3727c5ac
	v_cmp_ne_u32_e64 s[2:3], 1, v24
	global_load_dwordx4 v[96:99], v[0:1], off
	global_load_dwordx4 v[100:103], v[2:3], off
	global_load_dwordx4 v[104:107], v[0:1], off offset:1024
	global_load_dwordx4 v[108:111], v[2:3], off offset:1024
	global_load_dwordx4 v[112:115], v[0:1], off offset:2048
	global_load_dwordx4 v[116:119], v[2:3], off offset:2048
	global_load_dwordx4 v[120:123], v[0:1], off offset:3072
	global_load_dwordx4 v[124:127], v[2:3], off offset:3072
	global_load_dwordx4 v[128:131], v[4:5], off
	global_load_dwordx4 v[132:135], v[6:7], off
	global_load_dwordx4 v[136:139], v[8:9], off
	global_load_dwordx4 v[140:143], v[10:11], off
	global_load_dwordx4 v[144:147], v[12:13], off
	global_load_dwordx4 v[148:151], v[14:15], off
	global_load_dwordx4 v[152:155], v[16:17], off
	global_load_dwordx4 v[156:159], v[18:19], off
	s_branch .LBB0_16

; DI void ln_row_store(const float (&v)[32], int lane, const float* g, const float* b, float* outf, bf16_t* outb) {
;   float s = 0.f;
; #pragma unroll
;   for (int i = 0; i < 32; ++i) s += v[i];
;   s = wave_sum(s);
;   const float mu = s * (1.f / 2048.f);
;   float q = 0.f;
; #pragma unroll
;   for (int i = 0; i < 32; ++i) { const float d = v[i] - mu; q += d * d; }
;   q = wave_sum(q);
; DI void phase_ln_in(const Params& p, int bid, int nb) {
;     ...
;     const float* xr = p.x + (size_t)t * DM;
; #pragma unroll
;     for (int i = 0; i < 8; ++i) {
;       const float4 a = *(const float4*)(xr + (i * 64 + lane) * 4);
;       v[4 * i] = a.x; v[4 * i + 1] = a.y; v[4 * i + 2] = a.z; v[4 * i + 3] = a.w;
;     }
.LBB0_16:
	global_load_dwordx4 v[24:27], v[20:21], off offset:-4096
	global_load_dwordx4 v[28:31], v[20:21], off offset:-3072
	global_load_dwordx4 v[32:35], v[20:21], off offset:-2048
	global_load_dwordx4 v[36:39], v[20:21], off offset:-1024
	s_waitcnt lgkmcnt(0)
	global_load_dwordx4 v[64:67], v[20:21], off
	global_load_dwordx4 v[68:71], v[20:21], off offset:1024
	global_load_dwordx4 v[72:75], v[20:21], off offset:2048
	global_load_dwordx4 v[76:79], v[20:21], off offset:3072
	s_and_b64 vcc, exec, s[2:3]
	s_waitcnt vmcnt(7)
	v_add_f32_e32 v40, 0, v24
	v_add_f32_e32 v40, v25, v40
	v_add_f32_e32 v40, v26, v40
	v_add_f32_e32 v40, v27, v40
	s_waitcnt vmcnt(6)
	v_add_f32_e32 v40, v28, v40
	v_add_f32_e32 v40, v29, v40
	v_add_f32_e32 v40, v30, v40
	v_add_f32_e32 v40, v31, v40
	s_waitcnt vmcnt(5)
	v_add_f32_e32 v40, v32, v40
	v_add_f32_e32 v40, v33, v40
	v_add_f32_e32 v40, v34, v40
	v_add_f32_e32 v40, v35, v40
	s_waitcnt vmcnt(4)
	v_add_f32_e32 v40, v36, v40
	v_add_f32_e32 v40, v37, v40
	v_add_f32_e32 v40, v38, v40
	v_add_f32_e32 v40, v39, v40
	s_waitcnt vmcnt(3)
	v_add_f32_e32 v40, v64, v40
	v_add_f32_e32 v40, v65, v40
	v_add_f32_e32 v40, v66, v40
	v_add_f32_e32 v40, v67, v40
	s_waitcnt vmcnt(2)
	v_add_f32_e32 v40, v68, v40
	v_add_f32_e32 v40, v69, v40
	v_add_f32_e32 v40, v70, v40
	v_add_f32_e32 v40, v71, v40
	s_waitcnt vmcnt(1)
	v_add_f32_e32 v40, v72, v40
	v_add_f32_e32 v40, v73, v40
	v_add_f32_e32 v40, v74, v40
	v_add_f32_e32 v40, v75, v40
	s_waitcnt vmcnt(0)
	v_add_f32_e32 v40, v76, v40
	v_add_f32_e32 v40, v77, v40
	v_add_f32_e32 v40, v78, v40
	v_add_f32_e32 v40, v79, v40
	ds_bpermute_b32 v41, v57, v40
	s_waitcnt lgkmcnt(0)
	v_add_f32_e32 v40, v40, v41
	ds_bpermute_b32 v41, v58, v40
	s_waitcnt lgkmcnt(0)
	v_add_f32_e32 v40, v40, v41
	ds_bpermute_b32 v41, v59, v40
	s_waitcnt lgkmcnt(0)
	v_add_f32_e32 v40, v40, v41
	ds_bpermute_b32 v41, v60, v40
	s_waitcnt lgkmcnt(0)
	v_add_f32_e32 v40, v40, v41
	ds_bpermute_b32 v41, v61, v40
	s_waitcnt lgkmcnt(0)
	v_add_f32_e32 v40, v40, v41
	ds_bpermute_b32 v41, v62, v40
	s_waitcnt lgkmcnt(0)
	v_add_f32_e32 v40, v40, v41
	v_mul_f32_e32 v80, 0x3a000000, v40
	v_pk_add_f32 v[52:53], v[24:25], v[80:81] op_sel_hi:[1,0] neg_lo:[0,1] neg_hi:[0,1]
	v_pk_add_f32 v[54:55], v[26:27], v[80:81] op_sel_hi:[1,0] neg_lo:[0,1] neg_hi:[0,1]
	v_pk_add_f32 v[40:41], v[36:37], v[80:81] op_sel_hi:[1,0] neg_lo:[0,1] neg_hi:[0,1]
	v_pk_add_f32 v[36:37], v[64:65], v[80:81] op_sel_hi:[1,0] neg_lo:[0,1] neg_hi:[0,1]
	v_pk_mul_f32 v[64:65], v[52:53], v[52:53]
	v_pk_add_f32 v[42:43], v[38:39], v[80:81] op_sel_hi:[1,0] neg_lo:[0,1] neg_hi:[0,1]
	v_pk_add_f32 v[38:39], v[66:67], v[80:81] op_sel_hi:[1,0] neg_lo:[0,1] neg_hi:[0,1]
	v_pk_mul_f32 v[66:67], v[54:55], v[54:55]
	v_add_f32_e32 v64, v64, v65
	v_pk_add_f32 v[48:49], v[28:29], v[80:81] op_sel_hi:[1,0] neg_lo:[0,1] neg_hi:[0,1]
	v_add_f32_e32 v64, v66, v64
	v_pk_add_f32 v[44:45], v[32:33], v[80:81] op_sel_hi:[1,0] neg_lo:[0,1] neg_hi:[0,1]
	v_pk_add_f32 v[32:33], v[68:69], v[80:81] op_sel_hi:[1,0] neg_lo:[0,1] neg_hi:[0,1]
	v_pk_mul_f32 v[68:69], v[48:49], v[48:49]
	v_add_f32_e32 v64, v67, v64
	v_pk_add_f32 v[50:51], v[30:31], v[80:81] op_sel_hi:[1,0] neg_lo:[0,1] neg_hi:[0,1]
	v_add_f32_e32 v64, v68, v64
	v_pk_add_f32 v[46:47], v[34:35], v[80:81] op_sel_hi:[1,0] neg_lo:[0,1] neg_hi:[0,1]
	v_pk_add_f32 v[34:35], v[70:71], v[80:81] op_sel_hi:[1,0] neg_lo:[0,1] neg_hi:[0,1]
	v_pk_mul_f32 v[70:71], v[50:51], v[50:51]
	v_add_f32_e32 v66, v69, v64
	v_add_f32_e32 v66, v70, v66
	v_pk_add_f32 v[28:29], v[72:73], v[80:81] op_sel_hi:[1,0] neg_lo:[0,1] neg_hi:[0,1]
	v_pk_mul_f32 v[72:73], v[44:45], v[44:45]
	v_add_f32_e32 v66, v71, v66
	v_add_f32_e32 v66, v72, v66
	v_pk_add_f32 v[30:31], v[74:75], v[80:81] op_sel_hi:[1,0] neg_lo:[0,1] neg_hi:[0,1]
	v_pk_mul_f32 v[74:75], v[46:47], v[46:47]
	v_add_f32_e32 v66, v73, v66
	v_add_f32_e32 v66, v74, v66
	v_pk_add_f32 v[24:25], v[76:77], v[80:81] op_sel_hi:[1,0] neg_lo:[0,1] neg_hi:[0,1]
	v_pk_mul_f32 v[76:77], v[40:41], v[40:41]
	v_add_f32_e32 v66, v75, v66
	v_add_f32_e32 v66, v76, v66
	v_pk_add_f32 v[26:27], v[78:79], v[80:81] op_sel_hi:[1,0] neg_lo:[0,1] neg_hi:[0,1]
	v_pk_mul_f32 v[78:79], v[42:43], v[42:43]
	v_add_f32_e32 v66, v77, v66
	v_add_f32_e32 v66, v78, v66
	v_pk_mul_f32 v[80:81], v[36:37], v[36:37]
	v_add_f32_e32 v66, v79, v66
	v_add_f32_e32 v66, v80, v66
	v_pk_mul_f32 v[82:83], v[38:39], v[38:39]
	v_add_f32_e32 v66, v81, v66
	v_add_f32_e32 v66, v82, v66
	v_pk_mul_f32 v[84:85], v[32:33], v[32:33]
	v_add_f32_e32 v66, v83, v66
	v_add_f32_e32 v66, v84, v66
	v_pk_mul_f32 v[86:87], v[34:35], v[34:35]
	v_add_f32_e32 v66, v85, v66
	v_add_f32_e32 v66, v86, v66
	v_pk_mul_f32 v[88:89], v[28:29], v[28:29]
	v_add_f32_e32 v66, v87, v66
	v_add_f32_e32 v66, v88, v66
	v_pk_mul_f32 v[90:91], v[30:31], v[30:31]
	v_add_f32_e32 v66, v89, v66
	v_add_f32_e32 v66, v90, v66
	v_pk_mul_f32 v[92:93], v[24:25], v[24:25]
	v_add_f32_e32 v66, v91, v66
	v_add_f32_e32 v66, v92, v66
	v_pk_mul_f32 v[64:65], v[26:27], v[26:27]
	v_add_f32_e32 v66, v93, v66
	v_add_f32_e32 v64, v64, v66
	v_add_f32_e32 v64, v65, v64
	ds_bpermute_b32 v65, v57, v64
	s_waitcnt lgkmcnt(0)
	v_add_f32_e32 v64, v64, v65
	ds_bpermute_b32 v65, v58, v64
	s_waitcnt lgkmcnt(0)
	v_add_f32_e32 v64, v64, v65
	ds_bpermute_b32 v65, v59, v64
	s_waitcnt lgkmcnt(0)
	v_add_f32_e32 v64, v64, v65
	ds_bpermute_b32 v65, v60, v64
	s_waitcnt lgkmcnt(0)
	v_add_f32_e32 v64, v64, v65
	ds_bpermute_b32 v65, v61, v64
	s_waitcnt lgkmcnt(0)
	v_add_f32_e32 v64, v64, v65
	ds_bpermute_b32 v65, v62, v64
	s_cbranch_vccnz .LBB0_15
; DI void ln_row_store(const float (&v)[32], int lane, const float* g, const float* b, float* outf, bf16_t* outb) {
;     ...
;   const float rs = rsqrtf(q * (1.f / 2048.f) + LN_EPS);
; #pragma unroll
;   for (int i = 0; i < 8; ++i) {
;     const int c = (i * 64 + lane) * 4;
;     const float4 gg = *(const float4*)(g + c);
;     const float4 bb = *(const float4*)(b + c);
;     float4 o;
;     o.x = (v[4 * i + 0] - mu) * rs * gg.x + bb.x;
;     o.y = (v[4 * i + 1] - mu) * rs * gg.y + bb.y;
;     o.z = (v[4 * i + 2] - mu) * rs * gg.z + bb.z;
;     o.w = (v[4 * i + 3] - mu) * rs * gg.w + bb.w;
;     if (outf) *(float4*)(outf + c) = o;
;     if (outb) { uint2 pk; pk.x = pack2(o.x, o.y); pk.y = pack2(o.z, o.w); *(uint2*)(outb + c) = pk; }
;   }
	s_waitcnt lgkmcnt(0)
	v_add_f32_e32 v64, v64, v65
	v_fmamk_f32 v64, v64, 0x3a000000, v63
	s_mov_b32 s0, 0x800000
	v_mul_f32_e32 v65, 0x4b800000, v64
	v_cmp_gt_f32_e32 vcc, s0, v64
	s_nop 1
	v_cndmask_b32_e32 v64, v64, v65, vcc
	v_rsq_f32_e32 v64, v64
	s_nop 0
	v_mul_f32_e32 v65, 0x45800000, v64
	v_cndmask_b32_e32 v74, v64, v65, vcc
	v_pk_mul_f32 v[54:55], v[54:55], v[74:75] op_sel_hi:[1,0]
	v_pk_mul_f32 v[52:53], v[52:53], v[74:75] op_sel_hi:[1,0]
	v_pk_mul_f32 v[50:51], v[50:51], v[74:75] op_sel_hi:[1,0]
	v_pk_mul_f32 v[48:49], v[48:49], v[74:75] op_sel_hi:[1,0]
	v_pk_mul_f32 v[46:47], v[46:47], v[74:75] op_sel_hi:[1,0]
	v_pk_mul_f32 v[44:45], v[44:45], v[74:75] op_sel_hi:[1,0]
	v_pk_mul_f32 v[42:43], v[42:43], v[74:75] op_sel_hi:[1,0]
	v_pk_mul_f32 v[40:41], v[40:41], v[74:75] op_sel_hi:[1,0]
	v_pk_mul_f32 v[38:39], v[38:39], v[74:75] op_sel_hi:[1,0]
	v_pk_mul_f32 v[36:37], v[36:37], v[74:75] op_sel_hi:[1,0]
	v_pk_mul_f32 v[34:35], v[34:35], v[74:75] op_sel_hi:[1,0]
	v_pk_mul_f32 v[32:33], v[32:33], v[74:75] op_sel_hi:[1,0]
	v_pk_mul_f32 v[30:31], v[30:31], v[74:75] op_sel_hi:[1,0]
	v_pk_mul_f32 v[28:29], v[28:29], v[74:75] op_sel_hi:[1,0]
	v_pk_mul_f32 v[26:27], v[26:27], v[74:75] op_sel_hi:[1,0]
	v_pk_mul_f32 v[24:25], v[24:25], v[74:75] op_sel_hi:[1,0]
	v_pk_fma_f32 v[54:55], v[54:55], v[98:99], v[102:103]
	v_pk_fma_f32 v[52:53], v[52:53], v[96:97], v[100:101]
	s_nop 0
	v_cvt_pk_bf16_f32 v52, v52, v53
	v_cvt_pk_bf16_f32 v53, v54, v55
	global_store_dwordx2 v[22:23], v[52:53], off
	v_pk_fma_f32 v[50:51], v[50:51], v[106:107], v[110:111]
	v_pk_fma_f32 v[48:49], v[48:49], v[104:105], v[108:109]
	s_nop 0
	v_cvt_pk_bf16_f32 v48, v48, v49
	v_cvt_pk_bf16_f32 v49, v50, v51
	global_store_dwordx2 v[22:23], v[48:49], off offset:512
	v_pk_fma_f32 v[46:47], v[46:47], v[114:115], v[118:119]
	v_pk_fma_f32 v[44:45], v[44:45], v[112:113], v[116:117]
	s_nop 0
	v_cvt_pk_bf16_f32 v44, v44, v45
	v_cvt_pk_bf16_f32 v45, v46, v47
	global_store_dwordx2 v[22:23], v[44:45], off offset:1024
	v_pk_fma_f32 v[42:43], v[42:43], v[122:123], v[126:127]
	v_pk_fma_f32 v[40:41], v[40:41], v[120:121], v[124:125]
	s_nop 0
	v_cvt_pk_bf16_f32 v40, v40, v41
	v_cvt_pk_bf16_f32 v41, v42, v43
	global_store_dwordx2 v[22:23], v[40:41], off offset:1536
	v_pk_fma_f32 v[38:39], v[38:39], v[130:131], v[134:135]
	v_pk_fma_f32 v[36:37], v[36:37], v[128:129], v[132:133]
	s_nop 0
	v_cvt_pk_bf16_f32 v36, v36, v37
	v_cvt_pk_bf16_f32 v37, v38, v39
	global_store_dwordx2 v[22:23], v[36:37], off offset:2048
	v_pk_fma_f32 v[34:35], v[34:35], v[138:139], v[142:143]
	v_pk_fma_f32 v[32:33], v[32:33], v[136:137], v[140:141]
	s_nop 0
	v_cvt_pk_bf16_f32 v32, v32, v33
	v_cvt_pk_bf16_f32 v33, v34, v35
	global_store_dwordx2 v[22:23], v[32:33], off offset:2560
	v_pk_fma_f32 v[30:31], v[30:31], v[146:147], v[150:151]
	v_pk_fma_f32 v[28:29], v[28:29], v[144:145], v[148:149]
	s_nop 0
	v_cvt_pk_bf16_f32 v28, v28, v29
	v_cvt_pk_bf16_f32 v29, v30, v31
	global_store_dwordx2 v[22:23], v[28:29], off offset:3072
	v_pk_fma_f32 v[26:27], v[26:27], v[154:155], v[158:159]
	v_pk_fma_f32 v[24:25], v[24:25], v[152:153], v[156:157]
	s_nop 0
	v_cvt_pk_bf16_f32 v24, v24, v25
	v_cvt_pk_bf16_f32 v25, v26, v27
	global_store_dwordx2 v[22:23], v[24:25], off offset:3584
	s_branch .LBB0_15

; DI float bflo(unsigned u) { return __uint_as_float(u << 16); }
; DI float bfhi(unsigned u) { return __uint_as_float(u & 0xffff0000u); }
; #define OPAQUE_TID(P) (((P).wid0 << 6) | lane_id_now())
; DI void phase_final(const Params& p, int bid, int nb) {
;   const int tid_ = OPAQUE_TID(p), lane = tid_ & 63, wv = tid_ >> 6;
;   for (int t = bid * NWAVES + wv; t < NTOK; t += nb * NWAVES) {
;     float v[32];
;     const bf16_t* hr = p.h1b + (size_t)t * DM;
; #pragma unroll
;     for (int i = 0; i < 4; ++i) {
;       const int c = (i * 64 + lane) * 8;
;       const u32x4 ab = *(const u32x4*)(hr + c);
;       float s[8];
;       s[0] = DN_ALPHA * bflo(ab.x); s[1] = DN_ALPHA * bfhi(ab.x); s[2] = DN_ALPHA * bflo(ab.y); s[3] = DN_ALPHA * bfhi(ab.y);
;       s[4] = DN_ALPHA * bflo(ab.z); s[5] = DN_ALPHA * bfhi(ab.z); s[6] = DN_ALPHA * bflo(ab.w); s[7] = DN_ALPHA * bfhi(ab.w);
; #pragma unroll
;       for (int k = 0; k < 4; ++k) {
;         const u32x4 y = *(const u32x4*)(p.yb + (size_t)(t * 4 + k) * 2048 + c);
;     ...
;         const float4 gg = *(const float4*)(p.ln_ffn_g + c + 4 * h);
;         const float4 bb = *(const float4*)(p.ln_ffn_b + c + 4 * h);
.LBB0_1778:
	s_or_b64 exec, exec, s[0:1]
	v_readlane_b32 s0, v254, 14
	s_waitcnt lgkmcnt(0)
	s_barrier
	v_mbcnt_lo_u32_b32 v2, -1, 0
	v_mbcnt_hi_u32_b32 v2, -1, v2
	s_nop 0
	v_or_b32_e32 v0, s0, v2
	v_ashrrev_i32_e32 v0, 6, v0
	s_waitcnt vmcnt(3)
	v_add_u32_e32 v136, s38, v0
	s_movk_i32 s0, 0x2000
	v_cmp_gt_i32_e32 vcc, s0, v136
	s_and_saveexec_b64 s[0:1], vcc
	s_cbranch_execz .LBB0_1781
	v_mbcnt_lo_u32_b32 v3, -1, 0
	v_mbcnt_hi_u32_b32 v3, -1, v3
	v_and_b32_e32 v4, 64, v3
	v_add_u32_e32 v4, 64, v4
	v_xor_b32_e32 v5, 32, v3
	v_cmp_lt_i32_e32 vcc, v5, v4
	v_lshlrev_b32_e32 v1, 3, v2
	v_and_b32_e32 v1, 0x1f8, v1
	v_cndmask_b32_e32 v5, v3, v5, vcc
	v_lshlrev_b32_e32 v137, 2, v5
	v_xor_b32_e32 v5, 16, v3
	v_cmp_lt_i32_e32 vcc, v5, v4
	v_lshlrev_b32_e32 v6, 1, v1
	v_mov_b32_e32 v7, 0
	v_cndmask_b32_e32 v5, v3, v5, vcc
	v_lshlrev_b32_e32 v138, 2, v5
	v_xor_b32_e32 v5, 8, v3
	v_cmp_lt_i32_e32 vcc, v5, v4
	v_readlane_b32 s4, v254, 2
	v_lshl_add_u64 v[64:65], s[40:41], 0, v[6:7]
	v_cndmask_b32_e32 v5, v3, v5, vcc
	v_lshlrev_b32_e32 v139, 2, v5
	v_xor_b32_e32 v5, 4, v3
	v_cmp_lt_i32_e32 vcc, v5, v4
	v_readlane_b32 s5, v254, 3
	v_readlane_b32 s6, v254, 4
	v_cndmask_b32_e32 v5, v3, v5, vcc
	s_waitcnt vmcnt(2)
	v_lshlrev_b32_e32 v140, 2, v5
	v_xor_b32_e32 v5, 2, v3
	v_cmp_lt_i32_e32 vcc, v5, v4
	v_readlane_b32 s7, v254, 5
	s_ashr_i32 s39, s38, 31
	v_cndmask_b32_e32 v5, v3, v5, vcc
	v_lshlrev_b32_e32 v141, 2, v5
	v_xor_b32_e32 v5, 1, v3
	v_cmp_lt_i32_e32 vcc, v5, v4
	v_lshlrev_b32_e32 v4, 2, v1
	v_lshlrev_b32_e32 v1, 2, v0
	v_lshl_add_u32 v1, s97, 5, v1
	v_or_b32_e32 v6, 0x1000, v4
	v_or_b32_e32 v78, 3, v1
	v_ashrrev_i32_e32 v1, 31, v0
	v_cndmask_b32_e32 v3, v3, v5, vcc
	v_mov_b32_e32 v5, v7
	v_lshl_add_u64 v[70:71], s[4:5], 0, v[6:7]
	v_lshl_add_u64 v[72:73], s[6:7], 0, v[6:7]
	v_or_b32_e32 v6, 0x1800, v4
	v_lshl_add_u64 v[0:1], v[0:1], 0, s[38:39]
	v_lshl_add_u64 v[66:67], s[4:5], 0, v[4:5]
	v_lshl_add_u64 v[68:69], s[6:7], 0, v[4:5]
	v_lshl_add_u64 v[74:75], s[4:5], 0, v[6:7]
	v_lshl_add_u64 v[76:77], s[6:7], 0, v[6:7]
	v_lshlrev_b64 v[4:5], 13, v[0:1]
	v_and_b32_e32 v6, 63, v2
	v_readlane_b32 s2, v254, 0
	v_lshlrev_b64 v[0:1], 12, v[0:1]
	s_lshl_b32 s0, s96, 3
	v_lshl_or_b32 v4, v6, 5, v4
	v_readlane_b32 s3, v254, 1
	v_lshl_or_b32 v0, v6, 4, v0
	v_lshlrev_b32_e32 v142, 2, v3
	v_lshl_add_u64 v[2:3], s[2:3], 0, v[4:5]
	s_mov_b64 s[2:3], 0x1000
	s_ashr_i32 s1, s0, 31
	v_lshl_add_u64 v[0:1], s[88:89], 0, v[0:1]
	s_mov_b64 s[4:5], 0xc00
	s_lshl_b32 s9, s96, 5
	v_lshl_add_u64 v[80:81], v[2:3], 0, s[2:3]
	s_lshl_b64 s[2:3], s[0:1], 13
	v_lshl_add_u64 v[82:83], v[0:1], 0, s[4:5]
	s_lshl_b64 s[4:5], s[0:1], 12
	s_mov_b64 s[6:7], 0
	s_mov_b32 s8, 0x3f9837f0
	v_mov_b32_e32 v143, 0x3727c5ac
	s_mov_b32 s1, 0x800000
	s_movk_i32 s10, 0x1fff
	global_load_dwordx4 v[196:199], v[66:67], off offset:16
	global_load_dwordx4 v[200:203], v[68:69], off offset:16
	global_load_dwordx4 v[204:207], v[66:67], off offset:2048
	global_load_dwordx4 v[208:211], v[68:69], off offset:2048
	global_load_dwordx4 v[212:215], v[66:67], off offset:2064
	global_load_dwordx4 v[216:219], v[68:69], off offset:2064
	global_load_dwordx4 v[220:223], v[70:71], off
	global_load_dwordx4 v[224:227], v[72:73], off
	global_load_dwordx4 v[228:231], v[70:71], off offset:16
	global_load_dwordx4 v[232:235], v[72:73], off offset:16
	global_load_dwordx4 v[236:239], v[74:75], off
	global_load_dwordx4 v[240:243], v[76:77], off
	global_load_dwordx4 v[244:247], v[74:75], off offset:16
	global_load_dwordx4 v[248:251], v[76:77], off offset:16
.LBB0_1780:
	v_add_u32_e32 v8, -3, v78
	v_add_u32_e32 v10, -2, v78
	v_add_u32_e32 v12, -1, v78
	v_ashrrev_i32_e32 v79, 31, v78
	v_ashrrev_i32_e32 v9, 31, v8
	global_load_dwordx4 v[90:93], v[82:83], off offset:-3072
	global_load_dwordx4 v[100:103], v[82:83], off offset:-2048
	global_load_dwordx4 v[108:111], v[82:83], off offset:-1024
	v_ashrrev_i32_e32 v11, 31, v10
	v_ashrrev_i32_e32 v13, 31, v12
	v_lshlrev_b64 v[14:15], 12, v[78:79]
	v_lshlrev_b64 v[8:9], 12, v[8:9]
	global_load_dwordx4 v[116:119], v[82:83], off
	global_load_dwordx4 v[0:3], v[66:67], off
	global_load_dwordx4 v[4:7], v[68:69], off
	v_lshlrev_b64 v[10:11], 12, v[10:11]
	v_lshlrev_b64 v[12:13], 12, v[12:13]
	v_lshl_add_u64 v[14:15], v[64:65], 0, v[14:15]
	v_lshl_add_u64 v[84:85], v[64:65], 0, v[8:9]
	global_load_dwordx4 v[120:123], v[14:15], off
	global_load_dwordx4 v[128:131], v[14:15], off offset:1024
	global_load_dwordx4 v[60:63], v[14:15], off offset:2048
	global_load_dwordx4 v[56:59], v[14:15], off offset:3072
	v_lshl_add_u64 v[86:87], v[64:65], 0, v[10:11]
	v_lshl_add_u64 v[88:89], v[64:65], 0, v[12:13]
	global_load_dwordx4 v[52:55], v[84:85], off
	global_load_dwordx4 v[48:51], v[86:87], off
	global_load_dwordx4 v[44:47], v[88:89], off
	global_load_dwordx4 v[40:43], v[84:85], off offset:1024
	global_load_dwordx4 v[36:39], v[86:87], off offset:1024
	global_load_dwordx4 v[32:35], v[88:89], off offset:1024
	global_load_dwordx4 v[20:23], v[84:85], off offset:2048
	global_load_dwordx4 v[8:11], v[84:85], off offset:3072
	global_load_dwordx4 v[24:27], v[86:87], off offset:2048
	global_load_dwordx4 v[12:15], v[86:87], off offset:3072
	global_load_dwordx4 v[28:31], v[88:89], off offset:2048
	global_load_dwordx4 v[16:19], v[88:89], off offset:3072
	v_add_u32_e32 v136, s0, v136
	v_lshl_add_u64 v[82:83], v[82:83], 0, s[4:5]
	v_add_u32_e32 v78, s9, v78
	s_waitcnt vmcnt(21)
	v_lshlrev_b32_e32 v86, 16, v90
	v_and_b32_e32 v87, 0xffff0000, v90
	v_lshlrev_b32_e32 v88, 16, v91
	v_and_b32_e32 v89, 0xffff0000, v91
	s_waitcnt vmcnt(11)
; DI float bflo(unsigned u) { return __uint_as_float(u << 16); }
; DI float bfhi(unsigned u) { return __uint_as_float(u & 0xffff0000u); }
; DI void phase_final(const Params& p, int bid, int nb) {
;     ...
;     for (int i = 0; i < 4; ++i) {
;       const int c = (i * 64 + lane) * 8;
;       const u32x4 ab = *(const u32x4*)(hr + c);
;       float s[8];
;       s[0] = DN_ALPHA * bflo(ab.x); s[1] = DN_ALPHA * bfhi(ab.x); s[2] = DN_ALPHA * bflo(ab.y); s[3] = DN_ALPHA * bfhi(ab.y);
;       s[4] = DN_ALPHA * bflo(ab.z); s[5] = DN_ALPHA * bfhi(ab.z); s[6] = DN_ALPHA * bflo(ab.w); s[7] = DN_ALPHA * bfhi(ab.w);
; #pragma unroll
;       for (int k = 0; k < 4; ++k) {
;         const u32x4 y = *(const u32x4*)(p.yb + (size_t)(t * 4 + k) * 2048 + c);
;         s[0] += bflo(y.x); s[1] += bfhi(y.x); s[2] += bflo(y.y); s[3] += bfhi(y.y);
;         s[4] += bflo(y.z); s[5] += bfhi(y.z); s[6] += bflo(y.w); s[7] += bfhi(y.w);
;       }
; #pragma unroll
;       for (int j = 0; j < 8; ++j) v[8 * i + j] = s[j];
	v_lshlrev_b32_e32 v148, 16, v52
	v_and_b32_e32 v149, 0xffff0000, v52
	v_lshlrev_b32_e32 v112, 16, v116
	v_and_b32_e32 v113, 0xffff0000, v116
	v_lshlrev_b32_e32 v114, 16, v117
	v_and_b32_e32 v115, 0xffff0000, v117
	v_lshlrev_b32_e32 v116, 16, v118
	v_and_b32_e32 v117, 0xffff0000, v118
	v_lshlrev_b32_e32 v118, 16, v119
	v_and_b32_e32 v119, 0xffff0000, v119
	s_waitcnt vmcnt(10)
	v_lshlrev_b32_e32 v150, 16, v48
	v_and_b32_e32 v151, 0xffff0000, v48
	s_waitcnt vmcnt(4)
	v_lshlrev_b32_e32 v190, 16, v10
	v_and_b32_e32 v191, 0xffff0000, v10
	v_lshlrev_b32_e32 v10, 16, v11
	v_and_b32_e32 v11, 0xffff0000, v11
	v_pk_fma_f32 v[86:87], v[86:87], s[8:9], v[148:149] op_sel_hi:[1,0,1]
	v_lshlrev_b32_e32 v90, 16, v92
	v_and_b32_e32 v91, 0xffff0000, v92
	v_lshlrev_b32_e32 v92, 16, v93
	v_and_b32_e32 v93, 0xffff0000, v93
	v_lshlrev_b32_e32 v94, 16, v100
	v_and_b32_e32 v95, 0xffff0000, v100
	v_lshlrev_b32_e32 v98, 16, v101
	v_and_b32_e32 v99, 0xffff0000, v101
	v_lshlrev_b32_e32 v100, 16, v102
	v_and_b32_e32 v101, 0xffff0000, v102
	v_lshlrev_b32_e32 v152, 16, v44
	v_and_b32_e32 v153, 0xffff0000, v44
	v_lshlrev_b32_e32 v52, 16, v53
	v_and_b32_e32 v53, 0xffff0000, v53
	v_lshlrev_b32_e32 v154, 16, v54
	v_and_b32_e32 v155, 0xffff0000, v54
	v_lshlrev_b32_e32 v54, 16, v55
	v_and_b32_e32 v55, 0xffff0000, v55
	v_lshlrev_b32_e32 v160, 16, v40
	v_and_b32_e32 v161, 0xffff0000, v40
	v_lshlrev_b32_e32 v40, 16, v41
	v_and_b32_e32 v41, 0xffff0000, v41
	v_lshlrev_b32_e32 v166, 16, v42
	v_and_b32_e32 v167, 0xffff0000, v42
	s_waitcnt vmcnt(2)
	v_lshlrev_b32_e32 v192, 16, v14
	v_and_b32_e32 v193, 0xffff0000, v14
	v_lshlrev_b32_e32 v14, 16, v15
	v_and_b32_e32 v15, 0xffff0000, v15
	v_pk_fma_f32 v[10:11], v[118:119], s[8:9], v[10:11] op_sel_hi:[1,0,1]
	v_pk_add_f32 v[86:87], v[86:87], v[150:151]
	v_lshlrev_b32_e32 v84, 16, v120
	v_and_b32_e32 v85, 0xffff0000, v120
	v_lshlrev_b32_e32 v48, 16, v49
	v_and_b32_e32 v49, 0xffff0000, v49
	v_lshlrev_b32_e32 v162, 16, v36
	v_and_b32_e32 v163, 0xffff0000, v36
	v_lshlrev_b32_e32 v36, 16, v37
	v_and_b32_e32 v37, 0xffff0000, v37
	v_lshlrev_b32_e32 v168, 16, v38
	v_and_b32_e32 v169, 0xffff0000, v38
	v_lshlrev_b32_e32 v184, 16, v8
	v_and_b32_e32 v185, 0xffff0000, v8
	v_lshlrev_b32_e32 v8, 16, v9
	v_and_b32_e32 v9, 0xffff0000, v9
	v_pk_fma_f32 v[52:53], v[88:89], s[8:9], v[52:53] op_sel_hi:[1,0,1]
	v_pk_fma_f32 v[54:55], v[92:93], s[8:9], v[54:55] op_sel_hi:[1,0,1]
	v_pk_fma_f32 v[40:41], v[98:99], s[8:9], v[40:41] op_sel_hi:[1,0,1]
	v_pk_fma_f32 v[92:93], v[100:101], s[8:9], v[166:167] op_sel_hi:[1,0,1]
	v_pk_add_f32 v[10:11], v[10:11], v[14:15]
	v_pk_add_f32 v[14:15], v[86:87], v[152:153]
	v_lshlrev_b32_e32 v44, 16, v45
	v_and_b32_e32 v45, 0xffff0000, v45
	v_lshlrev_b32_e32 v164, 16, v32
	v_and_b32_e32 v165, 0xffff0000, v32
	v_lshlrev_b32_e32 v32, 16, v33
	v_and_b32_e32 v33, 0xffff0000, v33
	v_lshlrev_b32_e32 v170, 16, v34
	v_and_b32_e32 v171, 0xffff0000, v34
	v_lshlrev_b32_e32 v186, 16, v12
	v_and_b32_e32 v187, 0xffff0000, v12
	v_lshlrev_b32_e32 v12, 16, v13
	v_and_b32_e32 v13, 0xffff0000, v13
	v_pk_fma_f32 v[8:9], v[114:115], s[8:9], v[8:9] op_sel_hi:[1,0,1]
	v_pk_add_f32 v[48:49], v[52:53], v[48:49]
	v_pk_add_f32 v[36:37], v[40:41], v[36:37]
	v_pk_add_f32 v[40:41], v[92:93], v[168:169]
	v_pk_add_f32 v[14:15], v[14:15], v[84:85]
	v_lshlrev_b32_e32 v96, 16, v121
	v_and_b32_e32 v97, 0xffff0000, v121
	v_lshlrev_b32_e32 v156, 16, v50
	v_and_b32_e32 v157, 0xffff0000, v50
	s_waitcnt vmcnt(0)
	v_lshlrev_b32_e32 v188, 16, v16
	v_and_b32_e32 v189, 0xffff0000, v16
	v_lshlrev_b32_e32 v16, 16, v17
	v_and_b32_e32 v17, 0xffff0000, v17
	v_pk_fma_f32 v[88:89], v[90:91], s[8:9], v[154:155] op_sel_hi:[1,0,1]
	v_pk_add_f32 v[8:9], v[8:9], v[12:13]
	v_pk_add_f32 v[44:45], v[48:49], v[44:45]
	v_pk_add_f32 v[32:33], v[36:37], v[32:33]
	v_pk_add_f32 v[36:37], v[40:41], v[170:171]
	v_add_f32_e32 v40, 0, v14
	v_lshlrev_b32_e32 v158, 16, v46
	v_and_b32_e32 v159, 0xffff0000, v46
	v_pk_add_f32 v[52:53], v[88:89], v[156:157]
	v_pk_add_f32 v[8:9], v[8:9], v[16:17]
	v_pk_add_f32 v[16:17], v[44:45], v[96:97]
	v_add_f32_e32 v40, v15, v40
	v_lshlrev_b32_e32 v106, 16, v109
	v_and_b32_e32 v107, 0xffff0000, v109
	v_lshlrev_b32_e32 v120, 16, v122
	v_and_b32_e32 v121, 0xffff0000, v122
	v_lshlrev_b32_e32 v50, 16, v51
	v_and_b32_e32 v51, 0xffff0000, v51
	v_lshlrev_b32_e32 v172, 16, v20
	v_and_b32_e32 v173, 0xffff0000, v20
	v_lshlrev_b32_e32 v20, 16, v21
	v_and_b32_e32 v21, 0xffff0000, v21
	v_lshlrev_b32_e32 v194, 16, v18
	v_and_b32_e32 v195, 0xffff0000, v18
	v_lshlrev_b32_e32 v18, 16, v19
	v_and_b32_e32 v19, 0xffff0000, v19
	v_pk_add_f32 v[48:49], v[52:53], v[158:159]
	v_add_f32_e32 v40, v16, v40
	v_lshlrev_b32_e32 v46, 16, v47
	v_and_b32_e32 v47, 0xffff0000, v47
	v_lshlrev_b32_e32 v174, 16, v24
	v_and_b32_e32 v175, 0xffff0000, v24
	v_lshlrev_b32_e32 v24, 16, v25
	v_and_b32_e32 v25, 0xffff0000, v25
	v_pk_fma_f32 v[20:21], v[106:107], s[8:9], v[20:21] op_sel_hi:[1,0,1]
	v_pk_add_f32 v[50:51], v[54:55], v[50:51]
	v_pk_add_f32 v[10:11], v[10:11], v[18:19]
	v_pk_add_f32 v[18:19], v[48:49], v[120:121]
	v_add_f32_e32 v40, v17, v40
	v_lshlrev_b32_e32 v104, 16, v108
	v_and_b32_e32 v105, 0xffff0000, v108
	v_lshlrev_b32_e32 v108, 16, v110
	v_and_b32_e32 v109, 0xffff0000, v110
	v_lshlrev_b32_e32 v110, 16, v111
	v_and_b32_e32 v111, 0xffff0000, v111
	v_lshlrev_b32_e32 v122, 16, v123
	v_and_b32_e32 v123, 0xffff0000, v123
	v_lshlrev_b32_e32 v176, 16, v28
	v_and_b32_e32 v177, 0xffff0000, v28
	v_lshlrev_b32_e32 v28, 16, v29
	v_and_b32_e32 v29, 0xffff0000, v29
	v_lshlrev_b32_e32 v178, 16, v22
	v_and_b32_e32 v179, 0xffff0000, v22
	v_lshlrev_b32_e32 v22, 16, v23
	v_and_b32_e32 v23, 0xffff0000, v23
; DI float bflo(unsigned u) { return __uint_as_float(u << 16); }
; DI float bfhi(unsigned u) { return __uint_as_float(u & 0xffff0000u); }
; DI void phase_final(const Params& p, int bid, int nb) {
;     ...
; #pragma unroll
;       for (int k = 0; k < 4; ++k) {
;         const u32x4 y = *(const u32x4*)(p.yb + (size_t)(t * 4 + k) * 2048 + c);
;         s[0] += bflo(y.x); s[1] += bfhi(y.x); s[2] += bflo(y.y); s[3] += bfhi(y.y);
;         s[4] += bflo(y.z); s[5] += bfhi(y.z); s[6] += bflo(y.w); s[7] += bfhi(y.w);
;       }
; #pragma unroll
;       for (int j = 0; j < 8; ++j) v[8 * i + j] = s[j];
;     }
;     float sum = 0.f;
; #pragma unroll
;     for (int i = 0; i < 32; ++i) sum += v[i];
;     sum = wave_sum(sum);
	v_pk_fma_f32 v[90:91], v[94:95], s[8:9], v[160:161] op_sel_hi:[1,0,1]
	v_pk_add_f32 v[20:21], v[20:21], v[24:25]
	v_pk_add_f32 v[46:47], v[50:51], v[46:47]
	v_add_f32_e32 v40, v18, v40
	v_lshlrev_b32_e32 v180, 16, v26
	v_and_b32_e32 v181, 0xffff0000, v26
	v_lshlrev_b32_e32 v26, 16, v27
	v_and_b32_e32 v27, 0xffff0000, v27
	v_pk_fma_f32 v[22:23], v[110:111], s[8:9], v[22:23] op_sel_hi:[1,0,1]
	v_pk_add_f32 v[54:55], v[90:91], v[162:163]
	v_pk_add_f32 v[20:21], v[20:21], v[28:29]
	v_pk_add_f32 v[28:29], v[46:47], v[122:123]
	v_add_f32_e32 v40, v19, v40
	v_lshlrev_b32_e32 v124, 16, v128
	v_and_b32_e32 v125, 0xffff0000, v128
	v_lshlrev_b32_e32 v182, 16, v30
	v_and_b32_e32 v183, 0xffff0000, v30
	v_lshlrev_b32_e32 v30, 16, v31
	v_and_b32_e32 v31, 0xffff0000, v31
	v_pk_add_f32 v[22:23], v[22:23], v[26:27]
	v_pk_add_f32 v[50:51], v[54:55], v[164:165]
	v_add_f32_e32 v40, v28, v40
	v_pk_add_f32 v[22:23], v[22:23], v[30:31]
	v_pk_add_f32 v[30:31], v[50:51], v[124:125]
	v_add_f32_e32 v40, v29, v40
	v_lshlrev_b32_e32 v126, 16, v129
	v_and_b32_e32 v127, 0xffff0000, v129
	v_add_f32_e32 v40, v30, v40
	v_lshlrev_b32_e32 v102, 16, v103
	v_and_b32_e32 v103, 0xffff0000, v103
	v_lshlrev_b32_e32 v42, 16, v43
	v_and_b32_e32 v43, 0xffff0000, v43
	v_pk_add_f32 v[32:33], v[32:33], v[126:127]
	v_add_f32_e32 v40, v31, v40
	v_lshlrev_b32_e32 v128, 16, v130
	v_and_b32_e32 v129, 0xffff0000, v130
	v_lshlrev_b32_e32 v38, 16, v39
	v_and_b32_e32 v39, 0xffff0000, v39
	v_pk_fma_f32 v[42:43], v[102:103], s[8:9], v[42:43] op_sel_hi:[1,0,1]
	v_add_f32_e32 v40, v32, v40
	v_lshlrev_b32_e32 v34, 16, v35
	v_and_b32_e32 v35, 0xffff0000, v35
	v_pk_add_f32 v[38:39], v[42:43], v[38:39]
	v_pk_add_f32 v[36:37], v[36:37], v[128:129]
	v_add_f32_e32 v40, v33, v40
	v_lshlrev_b32_e32 v130, 16, v131
	v_and_b32_e32 v131, 0xffff0000, v131
	v_pk_fma_f32 v[94:95], v[104:105], s[8:9], v[172:173] op_sel_hi:[1,0,1]
	v_pk_add_f32 v[34:35], v[38:39], v[34:35]
	v_add_f32_e32 v40, v36, v40
	v_pk_add_f32 v[42:43], v[94:95], v[174:175]
	v_pk_add_f32 v[34:35], v[34:35], v[130:131]
	v_add_f32_e32 v40, v37, v40
	v_lshlrev_b32_e32 v132, 16, v60
	v_and_b32_e32 v133, 0xffff0000, v60
	v_pk_add_f32 v[38:39], v[42:43], v[176:177]
	v_add_f32_e32 v40, v34, v40
	v_pk_add_f32 v[38:39], v[38:39], v[132:133]
	v_add_f32_e32 v40, v35, v40
	v_lshlrev_b32_e32 v60, 16, v61
	v_and_b32_e32 v61, 0xffff0000, v61
	v_pk_fma_f32 v[98:99], v[108:109], s[8:9], v[178:179] op_sel_hi:[1,0,1]
	v_add_f32_e32 v40, v38, v40
	v_pk_add_f32 v[24:25], v[98:99], v[180:181]
	v_pk_add_f32 v[20:21], v[20:21], v[60:61]
	v_add_f32_e32 v40, v39, v40
	v_lshlrev_b32_e32 v134, 16, v62
	v_and_b32_e32 v135, 0xffff0000, v62
	v_pk_add_f32 v[24:25], v[24:25], v[182:183]
	v_add_f32_e32 v40, v20, v40
	v_pk_add_f32 v[24:25], v[24:25], v[134:135]
	v_add_f32_e32 v40, v21, v40
	v_lshlrev_b32_e32 v62, 16, v63
	v_and_b32_e32 v63, 0xffff0000, v63
	v_pk_fma_f32 v[100:101], v[112:113], s[8:9], v[184:185] op_sel_hi:[1,0,1]
	v_add_f32_e32 v40, v24, v40
	v_pk_add_f32 v[26:27], v[100:101], v[186:187]
	v_pk_add_f32 v[22:23], v[22:23], v[62:63]
	v_add_f32_e32 v40, v25, v40
	v_lshlrev_b32_e32 v144, 16, v56
	v_and_b32_e32 v145, 0xffff0000, v56
	v_pk_add_f32 v[26:27], v[26:27], v[188:189]
	v_add_f32_e32 v40, v22, v40
	v_pk_add_f32 v[26:27], v[26:27], v[144:145]
	v_add_f32_e32 v40, v23, v40
	v_lshlrev_b32_e32 v56, 16, v57
	v_and_b32_e32 v57, 0xffff0000, v57
	v_pk_fma_f32 v[102:103], v[116:117], s[8:9], v[190:191] op_sel_hi:[1,0,1]
	v_add_f32_e32 v40, v26, v40
	v_pk_add_f32 v[12:13], v[102:103], v[192:193]
	v_pk_add_f32 v[8:9], v[8:9], v[56:57]
	v_add_f32_e32 v40, v27, v40
	v_lshlrev_b32_e32 v146, 16, v58
	v_and_b32_e32 v147, 0xffff0000, v58
	v_pk_add_f32 v[12:13], v[12:13], v[194:195]
	v_add_f32_e32 v40, v8, v40
	v_pk_add_f32 v[12:13], v[12:13], v[146:147]
	v_add_f32_e32 v40, v9, v40
	v_lshlrev_b32_e32 v58, 16, v59
	v_and_b32_e32 v59, 0xffff0000, v59
	v_add_f32_e32 v40, v12, v40
	v_pk_add_f32 v[10:11], v[10:11], v[58:59]
	v_add_f32_e32 v40, v13, v40
	v_add_f32_e32 v40, v10, v40
	v_add_f32_e32 v40, v11, v40
	ds_bpermute_b32 v41, v137, v40
	s_waitcnt lgkmcnt(0)
	v_add_f32_e32 v40, v40, v41
	ds_bpermute_b32 v41, v138, v40
	s_waitcnt lgkmcnt(0)
	v_add_f32_e32 v40, v40, v41
	ds_bpermute_b32 v41, v139, v40
	s_waitcnt lgkmcnt(0)
	v_add_f32_e32 v40, v40, v41
	ds_bpermute_b32 v41, v140, v40
	s_waitcnt lgkmcnt(0)
	v_add_f32_e32 v40, v40, v41
	ds_bpermute_b32 v41, v141, v40
	s_waitcnt lgkmcnt(0)
	v_add_f32_e32 v40, v40, v41
	ds_bpermute_b32 v41, v142, v40
	s_waitcnt lgkmcnt(0)
; DI void phase_final(const Params& p, int bid, int nb) {
;     ...
;     sum = wave_sum(sum);
;     const float mu = sum * (1.f / 2048.f);
;     float q = 0.f;
; #pragma unroll
;     for (int i = 0; i < 32; ++i) { const float d = v[i] - mu; q += d * d; }
;     q = wave_sum(q);
;     const float rs = rsqrtf(q * (1.f / 2048.f) + LN_EPS);
;     float* outr = p.out + (size_t)t * DM;
; #pragma unroll
;     for (int i = 0; i < 4; ++i) {
;       const int c = (i * 64 + lane) * 8;
; #pragma unroll
;       for (int h = 0; h < 2; ++h) {
;         const float4 gg = *(const float4*)(p.ln_ffn_g + c + 4 * h);
;         const float4 bb = *(const float4*)(p.ln_ffn_b + c + 4 * h);
;         float4 o;
;         o.x = (v[8 * i + 4 * h + 0] - mu) * rs * gg.x + bb.x;
;         o.y = (v[8 * i + 4 * h + 1] - mu) * rs * gg.y + bb.y;
;         o.z = (v[8 * i + 4 * h + 2] - mu) * rs * gg.z + bb.z;
;         o.w = (v[8 * i + 4 * h + 3] - mu) * rs * gg.w + bb.w;
;         *(float4*)(outr + c + 4 * h) = o;
;       }
;     }
	v_add_f32_e32 v40, v40, v41
	v_mul_f32_e32 v40, 0x3a000000, v40
	v_pk_add_f32 v[14:15], v[14:15], v[40:41] op_sel_hi:[1,0] neg_lo:[0,1] neg_hi:[0,1]
	v_pk_add_f32 v[16:17], v[16:17], v[40:41] op_sel_hi:[1,0] neg_lo:[0,1] neg_hi:[0,1]
	v_pk_add_f32 v[18:19], v[18:19], v[40:41] op_sel_hi:[1,0] neg_lo:[0,1] neg_hi:[0,1]
	v_pk_add_f32 v[28:29], v[28:29], v[40:41] op_sel_hi:[1,0] neg_lo:[0,1] neg_hi:[0,1]
	v_pk_add_f32 v[30:31], v[30:31], v[40:41] op_sel_hi:[1,0] neg_lo:[0,1] neg_hi:[0,1]
	v_pk_add_f32 v[32:33], v[32:33], v[40:41] op_sel_hi:[1,0] neg_lo:[0,1] neg_hi:[0,1]
	v_pk_add_f32 v[36:37], v[36:37], v[40:41] op_sel_hi:[1,0] neg_lo:[0,1] neg_hi:[0,1]
	v_pk_add_f32 v[34:35], v[34:35], v[40:41] op_sel_hi:[1,0] neg_lo:[0,1] neg_hi:[0,1]
	v_pk_add_f32 v[38:39], v[38:39], v[40:41] op_sel_hi:[1,0] neg_lo:[0,1] neg_hi:[0,1]
	v_pk_add_f32 v[20:21], v[20:21], v[40:41] op_sel_hi:[1,0] neg_lo:[0,1] neg_hi:[0,1]
	v_pk_add_f32 v[24:25], v[24:25], v[40:41] op_sel_hi:[1,0] neg_lo:[0,1] neg_hi:[0,1]
	v_pk_add_f32 v[22:23], v[22:23], v[40:41] op_sel_hi:[1,0] neg_lo:[0,1] neg_hi:[0,1]
	v_pk_add_f32 v[26:27], v[26:27], v[40:41] op_sel_hi:[1,0] neg_lo:[0,1] neg_hi:[0,1]
	v_pk_add_f32 v[8:9], v[8:9], v[40:41] op_sel_hi:[1,0] neg_lo:[0,1] neg_hi:[0,1]
	v_pk_add_f32 v[12:13], v[12:13], v[40:41] op_sel_hi:[1,0] neg_lo:[0,1] neg_hi:[0,1]
	v_pk_add_f32 v[10:11], v[10:11], v[40:41] op_sel_hi:[1,0] neg_lo:[0,1] neg_hi:[0,1]
	v_pk_mul_f32 v[40:41], v[14:15], v[14:15]
	v_pk_mul_f32 v[42:43], v[16:17], v[16:17]
	v_add_f32_e32 v40, v40, v41
	v_add_f32_e32 v40, v42, v40
	v_pk_mul_f32 v[44:45], v[18:19], v[18:19]
	v_add_f32_e32 v40, v43, v40
	v_add_f32_e32 v40, v44, v40
	v_pk_mul_f32 v[46:47], v[28:29], v[28:29]
	v_add_f32_e32 v40, v45, v40
	v_add_f32_e32 v40, v46, v40
	v_pk_mul_f32 v[48:49], v[30:31], v[30:31]
	v_add_f32_e32 v40, v47, v40
	v_add_f32_e32 v40, v48, v40
	v_pk_mul_f32 v[50:51], v[32:33], v[32:33]
	v_add_f32_e32 v40, v49, v40
	v_add_f32_e32 v40, v50, v40
	v_pk_mul_f32 v[52:53], v[36:37], v[36:37]
	v_add_f32_e32 v40, v51, v40
	v_add_f32_e32 v40, v52, v40
	v_pk_mul_f32 v[54:55], v[34:35], v[34:35]
	v_add_f32_e32 v40, v53, v40
	v_add_f32_e32 v40, v54, v40
	v_pk_mul_f32 v[56:57], v[38:39], v[38:39]
	v_add_f32_e32 v40, v55, v40
	v_add_f32_e32 v40, v56, v40
	v_pk_mul_f32 v[58:59], v[20:21], v[20:21]
	v_add_f32_e32 v40, v57, v40
	v_add_f32_e32 v40, v58, v40
	v_pk_mul_f32 v[60:61], v[24:25], v[24:25]
	v_add_f32_e32 v40, v59, v40
	v_add_f32_e32 v40, v60, v40
	v_pk_mul_f32 v[62:63], v[22:23], v[22:23]
	v_add_f32_e32 v40, v61, v40
	v_add_f32_e32 v40, v62, v40
	v_pk_mul_f32 v[84:85], v[26:27], v[26:27]
	v_add_f32_e32 v40, v63, v40
	v_add_f32_e32 v40, v84, v40
	v_pk_mul_f32 v[86:87], v[8:9], v[8:9]
	v_add_f32_e32 v40, v85, v40
	v_add_f32_e32 v40, v86, v40
	v_pk_mul_f32 v[88:89], v[12:13], v[12:13]
	v_add_f32_e32 v40, v87, v40
	v_add_f32_e32 v40, v88, v40
	v_pk_mul_f32 v[90:91], v[10:11], v[10:11]
	v_add_f32_e32 v40, v89, v40
	v_add_f32_e32 v40, v90, v40
	v_add_f32_e32 v40, v91, v40
	ds_bpermute_b32 v41, v137, v40
	s_waitcnt lgkmcnt(0)
	v_add_f32_e32 v40, v40, v41
	ds_bpermute_b32 v41, v138, v40
	s_waitcnt lgkmcnt(0)
	v_add_f32_e32 v40, v40, v41
	ds_bpermute_b32 v41, v139, v40
	s_waitcnt lgkmcnt(0)
	v_add_f32_e32 v40, v40, v41
	ds_bpermute_b32 v41, v140, v40
	s_waitcnt lgkmcnt(0)
	v_add_f32_e32 v40, v40, v41
	ds_bpermute_b32 v41, v141, v40
	s_waitcnt lgkmcnt(0)
	v_add_f32_e32 v40, v40, v41
	ds_bpermute_b32 v41, v142, v40
	s_waitcnt lgkmcnt(0)
	v_add_f32_e32 v40, v40, v41
	v_fmamk_f32 v40, v40, 0x3a000000, v143
	v_mul_f32_e32 v41, 0x4b800000, v40
	v_cmp_gt_f32_e32 vcc, s1, v40
	s_nop 1
	v_cndmask_b32_e32 v40, v40, v41, vcc
	v_rsq_f32_e32 v40, v40
	s_nop 0
	v_mul_f32_e32 v41, 0x45800000, v40
	v_cndmask_b32_e32 v40, v40, v41, vcc
	v_pk_mul_f32 v[14:15], v[14:15], v[40:41] op_sel_hi:[1,0]
	v_pk_mul_f32 v[16:17], v[16:17], v[40:41] op_sel_hi:[1,0]
	v_pk_fma_f32 v[0:1], v[0:1], v[14:15], v[4:5]
	v_pk_fma_f32 v[2:3], v[2:3], v[16:17], v[6:7]
	global_store_dwordx4 v[80:81], v[0:3], off offset:-4096
	v_cmp_lt_i32_e32 vcc, s10, v136
	s_or_b64 s[6:7], vcc, s[6:7]
	v_pk_mul_f32 v[44:45], v[18:19], v[40:41] op_sel_hi:[1,0]
	v_pk_mul_f32 v[46:47], v[28:29], v[40:41] op_sel_hi:[1,0]
	v_pk_fma_f32 v[44:45], v[196:197], v[44:45], v[200:201]
	v_pk_fma_f32 v[46:47], v[198:199], v[46:47], v[202:203]
	global_store_dwordx4 v[80:81], v[44:47], off offset:-4080
	v_pk_mul_f32 v[48:49], v[30:31], v[40:41] op_sel_hi:[1,0]
	v_pk_mul_f32 v[50:51], v[32:33], v[40:41] op_sel_hi:[1,0]
	v_pk_fma_f32 v[48:49], v[204:205], v[48:49], v[208:209]
	v_pk_fma_f32 v[50:51], v[206:207], v[50:51], v[210:211]
	global_store_dwordx4 v[80:81], v[48:51], off offset:-2048
	v_pk_mul_f32 v[52:53], v[36:37], v[40:41] op_sel_hi:[1,0]
	v_pk_mul_f32 v[54:55], v[34:35], v[40:41] op_sel_hi:[1,0]
	v_pk_fma_f32 v[52:53], v[212:213], v[52:53], v[216:217]
	v_pk_fma_f32 v[54:55], v[214:215], v[54:55], v[218:219]
	global_store_dwordx4 v[80:81], v[52:55], off offset:-2032
	v_pk_mul_f32 v[56:57], v[38:39], v[40:41] op_sel_hi:[1,0]
	v_pk_mul_f32 v[58:59], v[20:21], v[40:41] op_sel_hi:[1,0]
	v_pk_fma_f32 v[56:57], v[220:221], v[56:57], v[224:225]
	v_pk_fma_f32 v[58:59], v[222:223], v[58:59], v[226:227]
	global_store_dwordx4 v[80:81], v[56:59], off
	v_pk_mul_f32 v[60:61], v[24:25], v[40:41] op_sel_hi:[1,0]
	v_pk_mul_f32 v[62:63], v[22:23], v[40:41] op_sel_hi:[1,0]
	v_pk_fma_f32 v[60:61], v[228:229], v[60:61], v[232:233]
	v_pk_fma_f32 v[62:63], v[230:231], v[62:63], v[234:235]
	global_store_dwordx4 v[80:81], v[60:63], off offset:16
	v_pk_mul_f32 v[84:85], v[26:27], v[40:41] op_sel_hi:[1,0]
	v_pk_mul_f32 v[86:87], v[8:9], v[40:41] op_sel_hi:[1,0]
	v_pk_fma_f32 v[84:85], v[236:237], v[84:85], v[240:241]
	v_pk_fma_f32 v[86:87], v[238:239], v[86:87], v[242:243]
	global_store_dwordx4 v[80:81], v[84:87], off offset:2048
	v_pk_mul_f32 v[88:89], v[12:13], v[40:41] op_sel_hi:[1,0]
	v_pk_mul_f32 v[90:91], v[10:11], v[40:41] op_sel_hi:[1,0]
	v_pk_fma_f32 v[88:89], v[244:245], v[88:89], v[248:249]
	v_pk_fma_f32 v[90:91], v[246:247], v[90:91], v[250:251]
	global_store_dwordx4 v[80:81], v[88:91], off offset:2064
	v_lshl_add_u64 v[80:81], v[80:81], 0, s[2:3]
	s_andn2_b64 exec, exec, s[6:7]
	s_cbranch_execnz .LBB0_1780
